# baseline (speedup 1.0000x reference)
.LBB3_2:
	s_or_b64 exec, exec, s[4:5]
	s_load_dwordx2 s[18:19], s[0:1], 0x8
	s_load_dwordx4 s[4:7], s[0:1], 0x18
	s_movk_i32 s8, 0x100
	v_cmp_gt_u32_e64 s[50:51], s8, v0
	s_and_saveexec_b64 s[8:9], s[50:51]
	v_mov_b32_e32 v1, 0x21e00
	v_lshl_add_u32 v1, v0, 2, v1
	v_mov_b32_e32 v2, 0
	ds_write_b32 v1, v2
	s_or_b64 exec, exec, s[8:9]
	v_cmp_eq_u32_e32 vcc, 0, v0
	s_and_saveexec_b64 s[8:9], vcc
	v_mov_b32_e32 v1, 0
	v_mov_b32_e32 v2, 0x22c50
	ds_write_b32 v2, v1
	s_or_b64 exec, exec, s[8:9]
	v_and_b32_e32 v18, 63, v0
	v_lshlrev_b32_e32 v1, 3, v18
	s_lshl_b32 s30, s3, 2
	s_waitcnt lgkmcnt(0)
	global_load_dwordx2 v[12:13], v1, s[4:5] offset:1024
	global_load_dwordx2 v[6:7], v1, s[4:5] offset:1536
	global_load_dwordx2 v[14:15], v1, s[4:5]
	global_load_dwordx2 v[16:17], v1, s[6:7]
	global_load_dwordx2 v[8:9], v1, s[4:5] offset:512
	global_load_dwordx2 v[10:11], v1, s[6:7] offset:512
	v_and_b32_e32 v63, 31, v0
	v_lshlrev_b32_e32 v63, 2, v63
	global_load_dword v64, v63, s[4:5] offset:0
	global_load_dword v65, v63, s[4:5] offset:1024
	global_load_dword v66, v63, s[6:7] offset:0
	global_load_dword v68, v63, s[4:5] offset:128
	global_load_dword v69, v63, s[4:5] offset:1152
	global_load_dword v70, v63, s[6:7] offset:128
	global_load_dword v72, v63, s[4:5] offset:256
	global_load_dword v73, v63, s[4:5] offset:1280
	global_load_dword v74, v63, s[6:7] offset:256
	global_load_dword v76, v63, s[4:5] offset:384
	global_load_dword v77, v63, s[4:5] offset:1408
	global_load_dword v78, v63, s[6:7] offset:384
	global_load_dword v80, v63, s[4:5] offset:512
	global_load_dword v81, v63, s[4:5] offset:1536
	global_load_dword v82, v63, s[6:7] offset:512
	global_load_dword v84, v63, s[4:5] offset:640
	global_load_dword v85, v63, s[4:5] offset:1664
	global_load_dword v86, v63, s[6:7] offset:640
	global_load_dword v88, v63, s[4:5] offset:768
	global_load_dword v89, v63, s[4:5] offset:1792
	global_load_dword v90, v63, s[6:7] offset:768
	global_load_dword v92, v63, s[4:5] offset:896
	global_load_dword v93, v63, s[4:5] offset:1920
	global_load_dword v94, v63, s[6:7] offset:896
	s_add_i32 s4, s30, 0x228a0
	v_mov_b32_e32 v2, s4
	s_barrier
	v_mov_b32_e32 v1, 0x228a0
	ds_read_b32 v2, v2
	ds_read_b32 v20, v1
	v_or_b32_e32 v23, 0x400, v0
	v_or_b32_e32 v22, 0x800, v0
	v_or_b32_e32 v21, 0xc00, v0
	s_waitcnt lgkmcnt(1)
	v_readfirstlane_b32 s4, v2
	s_waitcnt lgkmcnt(0)
	v_readfirstlane_b32 s5, v20
	s_sub_i32 s25, s4, s5
	v_cmp_gt_i32_e32 vcc, s25, v0
	v_cmp_gt_i32_e64 s[6:7], s25, v23
	v_cmp_gt_i32_e64 s[8:9], s25, v22
	v_cndmask_b32_e32 v1, 0, v0, vcc
	v_add_u32_e32 v2, v1, v20
	v_cndmask_b32_e64 v1, 0, v23, s[6:7]
	v_add_u32_e32 v4, v1, v20
	v_cndmask_b32_e64 v1, 0, v22, s[8:9]
	v_add_u32_e32 v24, v1, v20
	v_cmp_gt_i32_e64 s[10:11], s25, v21
	v_ashrrev_i32_e32 v25, 31, v24
	v_ashrrev_i32_e32 v3, 31, v2
	v_cndmask_b32_e64 v1, 0, v21, s[10:11]
	v_lshl_add_u64 v[30:31], v[24:25], 2, s[18:19]
	v_add_u32_e32 v24, v1, v20
	v_lshl_add_u64 v[2:3], v[2:3], 2, s[18:19]
	v_ashrrev_i32_e32 v5, 31, v4
	v_ashrrev_i32_e32 v25, 31, v24
	v_lshl_add_u64 v[4:5], v[4:5], 2, s[18:19]
	v_lshl_add_u64 v[32:33], v[24:25], 2, s[18:19]
	global_load_dword v25, v[2:3], off
	global_load_dword v26, v[4:5], off
	global_load_dword v28, v[30:31], off
	global_load_dword v29, v[32:33], off
	v_cmp_gt_i32_e64 s[4:5], s3, v0
	s_and_saveexec_b64 s[12:13], s[4:5]
	s_cbranch_execz .LBB3_8
	v_lshlrev_b32_e32 v1, 2, v0
	v_add_u32_e32 v2, 0x228a0, v1
	ds_read2_b32 v[2:3], v2 offset1:1
	v_add_u32_e32 v1, 0x22580, v1
	s_waitcnt lgkmcnt(0)
	v_sub_u32_e32 v2, v3, v2
	v_add_u32_e32 v2, 3, v2
	v_ashrrev_i32_e32 v2, 2, v2
	ds_write_b32 v1, v2

.LBB3_39:
	v_cvt_f16_f32_e32 v3, v14
	v_cvt_f16_f32_e32 v4, v12
	v_mul_f32_e32 v21, v16, v2
	v_fma_mixlo_f16 v5, v16, v2, 0
	v_mul_u32_u24_e32 v16, 0x10001, v3
	v_mul_u32_u24_e32 v22, 0x10001, v4
	v_cvt_f16_f32_e32 v3, v15
	v_cvt_f16_f32_e32 v4, v13
	s_mov_b32 s0, 0x10001
	v_mul_u32_u24_sdwa v23, v5, s0 dst_sel:DWORD dst_unused:UNUSED_PAD src0_sel:WORD_0 src1_sel:DWORD
	v_mul_f32_e32 v24, v17, v2
	v_fma_mixlo_f16 v5, v17, v2, 0
	v_mul_u32_u24_e32 v17, 0x10001, v3
	v_mul_u32_u24_e32 v25, 0x10001, v4
	v_cvt_f16_f32_e32 v3, v8
	v_cvt_f16_f32_e32 v4, v6
	v_mul_u32_u24_sdwa v26, v5, s0 dst_sel:DWORD dst_unused:UNUSED_PAD src0_sel:WORD_0 src1_sel:DWORD
	v_mul_f32_e32 v27, v10, v2
	v_fma_mixlo_f16 v5, v10, v2, 0
	v_mul_u32_u24_e32 v10, 0x10001, v3
	v_mul_u32_u24_e32 v28, 0x10001, v4
	v_cvt_f16_f32_e32 v3, v9
	v_cvt_f16_f32_e32 v4, v7
	v_sub_u32_e32 v20, 0x7f000000, v2
	v_mul_f32_e32 v14, v14, v2
	v_mul_f32_e32 v12, v12, v2
	v_mul_f32_e32 v15, v15, v2
	v_mul_f32_e32 v13, v13, v2
	v_mul_u32_u24_sdwa v29, v5, s0 dst_sel:DWORD dst_unused:UNUSED_PAD src0_sel:WORD_0 src1_sel:DWORD
	v_mul_f32_e32 v8, v8, v2
	v_mul_f32_e32 v6, v6, v2
	v_mul_f32_e32 v30, v11, v2
	v_fma_mixlo_f16 v5, v11, v2, 0
	v_mul_f32_e32 v9, v9, v2
	v_mul_f32_e32 v7, v7, v2
	v_cndmask_b32_e64 v2, 0, 1, s[26:27]
	v_mul_u32_u24_e32 v11, 0x10001, v3
	v_mul_u32_u24_e32 v31, 0x10001, v4
	v_mul_u32_u24_sdwa v32, v5, s0 dst_sel:DWORD dst_unused:UNUSED_PAD src0_sel:WORD_0 src1_sel:DWORD
	v_lshlrev_b32_e32 v33, 1, v33
	v_mov_b32_e32 v34, 0x22c50
	v_cmp_ne_u32_e64 s[6:7], 1, v2
	s_movk_i32 s12, 0x3c00
	v_mov_b32_e32 v35, 0x3c00
	s_waitcnt lgkmcnt(0)
	s_barrier
	s_and_b64 vcc, exec, s[6:7]
	s_cbranch_vccz .LBB3_43
	s_waitcnt vmcnt(0)
	v_sub_u32_e32 v61, 0x7f000000, v20
	v_cvt_pk_f16_f32 v64, v64, v65
	v_mul_f32_e32 v66, v61, v66
	v_cvt_pk_f16_f32 v65, v66, 0
	v_mov_b32_e32 v66, 0
	v_mov_b32_e32 v67, 0
	v_cvt_pk_f16_f32 v68, v68, v69
	v_mul_f32_e32 v70, v61, v70
	v_cvt_pk_f16_f32 v69, v70, 0
	v_mov_b32_e32 v70, 0
	v_mov_b32_e32 v71, 0
	v_cvt_pk_f16_f32 v72, v72, v73
	v_mul_f32_e32 v74, v61, v74
	v_cvt_pk_f16_f32 v73, v74, 0
	v_mov_b32_e32 v74, 0
	v_mov_b32_e32 v75, 0
	v_cvt_pk_f16_f32 v76, v76, v77
	v_mul_f32_e32 v78, v61, v78
	v_cvt_pk_f16_f32 v77, v78, 0
	v_mov_b32_e32 v78, 0
	v_mov_b32_e32 v79, 0
	v_cvt_pk_f16_f32 v80, v80, v81
	v_mul_f32_e32 v82, v61, v82
	v_cvt_pk_f16_f32 v81, v82, 0
	v_mov_b32_e32 v82, 0
	v_mov_b32_e32 v83, 0
	v_cvt_pk_f16_f32 v84, v84, v85
	v_mul_f32_e32 v86, v61, v86
	v_cvt_pk_f16_f32 v85, v86, 0
	v_mov_b32_e32 v86, 0
	v_mov_b32_e32 v87, 0
	v_cvt_pk_f16_f32 v88, v88, v89
	v_mul_f32_e32 v90, v61, v90
	v_cvt_pk_f16_f32 v89, v90, 0
	v_mov_b32_e32 v90, 0
	v_mov_b32_e32 v91, 0
	v_cvt_pk_f16_f32 v92, v92, v93
	v_mul_f32_e32 v94, v61, v94
	v_cvt_pk_f16_f32 v93, v94, 0
	v_mov_b32_e32 v94, 0
	v_mov_b32_e32 v95, 0
	v_and_b32_e32 v63, 31, v18
	v_lshrrev_b32_e32 v55, 3, v63
	v_lshlrev_b32_e32 v56, 2, v55
	v_and_b32_e32 v57, 3, v63
	v_add_u32_e32 v56, v56, v57
	v_lshlrev_b32_e32 v55, 4, v55
	v_bfe_u32 v57, v63, 1, 1
	v_lshl_add_u32 v55, v57, 3, v55
	v_add_u32_e32 v55, 0x1ce00, v55
	v_and_b32_e32 v57, 1, v63
	v_cmp_eq_u32_e32 vcc, 1, v57
	v_mov_b32_e32 v57, 0x5040100
	v_mov_b32_e32 v10, 0x7060302
	v_lshlrev_b32_e32 v58, 1, v63
	v_cndmask_b32_e32 v57, v57, v10, vcc
	v_mov_b32_e32 v59, 0x22c50
	v_mov_b32_e32 v60, 1
	v_mov_b32_e32 v62, 0x3c003c00
	v_mov_b32_e32 v34, 0
	v_mov_b32_e32 v35, 0
	v_mov_b32_e32 v2, v55
	s_mov_b32 s52, 0x0f0f0f0f
	s_mov_b32 s53, 0
	s_mov_b32 s54, 0xf0f0f0f0
	s_mov_b32 s55, 0
	s_mov_b32 s56, 0
	s_mov_b32 s57, -1
	v_lshrrev_b32_e32 v10, 2, v0
	v_cmp_gt_u32_e32 vcc, s3, v10
	s_and_saveexec_b64 s[58:59], vcc
	s_cbranch_execz .Llin_skip
	v_lshlrev_b32_e32 v11, 2, v10
	v_add_u32_e32 v12, 0x228a0, v11
	v_add_u32_e32 v13, 0x22580, v11
	ds_read2_b32 v[14:15], v12 offset1:1
	ds_read_b32 v16, v13
	v_and_b32_e32 v17, 3, v0
	v_mov_b32_e32 v40, 0
	v_mov_b32_e32 v41, 0
	s_waitcnt lgkmcnt(0)
	v_sub_u32_e32 v14, v15, v14
	v_add_u32_e32 v14, 3, v14
	v_lshrrev_b32_e32 v14, 2, v14
	v_add_u32_e32 v15, v16, v14
	v_add_u32_e32 v16, v16, v17
	v_mov_b32_e32 v17, 0x1ce00
.Llin_loop:
	v_cmp_lt_u32_e32 vcc, v16, v15
	s_and_b64 exec, exec, vcc
	s_cbranch_execz .Llin_skip
	v_lshl_add_u32 v12, v16, 4, v17
	ds_read_b128 v[36:39], v12
	v_add_u32_e32 v16, 4, v16
	s_waitcnt lgkmcnt(0)
	v_dot2_f32_f16 v40, v36, v62, v40
	v_dot2_f32_f16 v41, v37, v62, v41
	v_dot2_f32_f16 v40, v38, v62, v40
	v_dot2_f32_f16 v41, v39, v62, v41
	s_branch .Llin_loop
.Llin_skip:
	s_mov_b64 exec, s[58:59]
	s_nop 4
	v_add_f32_dpp v40, v40, v40 quad_perm:[1,0,3,2] row_mask:0xf bank_mask:0xf
	v_add_f32_dpp v41, v41, v41 quad_perm:[1,0,3,2] row_mask:0xf bank_mask:0xf
	s_nop 1
	v_add_f32_dpp v40, v40, v40 quad_perm:[2,3,0,1] row_mask:0xf bank_mask:0xf
	v_add_f32_dpp v41, v41, v41 quad_perm:[2,3,0,1] row_mask:0xf bank_mask:0xf
	v_and_b32_e32 v12, 3, v0
	v_cmp_eq_u32_e32 vcc, 0, v12
	v_cmp_gt_u32_e64 s[60:61], s3, v10
	v_lshlrev_b32_e32 v12, 3, v10
	v_add_u32_e32 v12, 0x22c60, v12
	s_and_b64 vcc, vcc, s[60:61]
	s_and_saveexec_b64 s[60:61], vcc
	ds_write_b64 v12, v[40:41]
	s_mov_b64 exec, s[60:61]
	s_waitcnt lgkmcnt(0)
	s_barrier
.Lp_next:
	s_mov_b64 exec, 1
	ds_add_rtn_u32 v10, v59, v60
	s_mov_b64 exec, -1
	s_waitcnt lgkmcnt(0)
	v_readfirstlane_b32 s34, v10
	s_lshl_b32 s35, s34, 1
	s_cmp_ge_i32 s35, s3
	s_cbranch_scc1 .Lp_done
	s_lshl_b32 s45, s35, 2
	s_add_i32 s46, s45, 0x228a0
	v_mov_b32_e32 v11, s46
	s_add_i32 s46, s45, 0x22580
	v_mov_b32_e32 v12, s46
	s_lshl_b32 s46, s35, 3
	s_add_i32 s46, s46, 0x22c60
	v_mov_b32_e32 v13, s46
	ds_read2_b32 v[14:15], v11 offset1:1
	ds_read_b32 v16, v11 offset:8
	ds_read2_b32 v[36:37], v12 offset1:1
	ds_read_b128 v[40:43], v13
	s_waitcnt lgkmcnt(0)
	v_readfirstlane_b32 s36, v14
	v_readfirstlane_b32 s37, v15
	v_readfirstlane_b32 s38, v16
	v_readfirstlane_b32 s39, v36
	v_readfirstlane_b32 s40, v37
	s_sub_i32 s41, s37, s36
	s_sub_i32 s42, s38, s37
	s_add_i32 s45, s35, 1
	s_cmp_lt_i32 s45, s3
	s_cselect_b32 s42, s42, 0
	s_add_i32 s45, s41, 15
	s_lshr_b32 s45, s45, 4
	s_add_i32 s46, s42, 15
	s_lshr_b32 s46, s46, 4
	s_max_u32 s43, s45, s46
	s_add_i32 s45, s41, -1
	s_flbit_i32_b32 s45, s45
	s_sub_i32 s45, 32, s45
	s_cmp_gt_i32 s41, 1
	s_cselect_b32 s58, s45, 0
	s_lshl_b32 s58, s58, 23
	s_add_i32 s45, s42, -1
	s_flbit_i32_b32 s45, s45
	s_sub_i32 s45, 32, s45
	s_cmp_gt_i32 s42, 1
	s_cselect_b32 s59, s45, 0
	s_lshl_b32 s59, s59, 23
	s_sub_i32 s60, 0x46800000, s58
	s_sub_i32 s61, 0x46800000, s59
	s_add_i32 s58, s58, 0x38000000
	s_add_i32 s59, s59, 0x38000000
	v_mov_b32_e32 v5, v40
	v_mov_b32_e32 v6, v41
	v_cvt_f32_i32_e32 v7, s41
	v_mov_b32_e32 v8, s60
	s_mul_i32 s45, s35, 0x210
	v_add_u32_e32 v9, s45, v58
	s_mov_b64 exec, s[56:57]
	v_mov_b32_e32 v5, v42
	v_mov_b32_e32 v6, v43
	v_cvt_f32_i32_e32 v7, s42
	v_mov_b32_e32 v8, s61
	s_addk_i32 s45, 0x210
	v_add_u32_e32 v9, s45, v58
	s_mov_b64 exec, -1
	v_mov_b32_e32 v3, 0
	s_lshl_b32 s46, s39, 4
	s_lshl_b32 s47, s40, 4
	s_mov_b64 exec, s[52:53]
	v_mov_b32_e32 v3, s41
	v_add_u32_e32 v2, s46, v55
	s_mov_b64 exec, s[54:55]
	v_mov_b32_e32 v3, s42
	v_add_u32_e32 v2, s47, v55
	s_mov_b64 exec, -1
	v_mov_b32_e32 v4, v56
	v_mul_f32_e32 v10, s58, v20
	v_mul_f32_e32 v11, s59, v20
	s_lshl_b32 s45, s35, 2
	s_add_i32 s45, s45, 0x22200
	v_mov_b32_e32 v12, s45
	s_mov_b64 exec, 1
	ds_write2_b32 v12, v10, v11 offset1:1
	s_mov_b64 exec, -1
	v_mov_b32_e32 v24, 0
	v_mov_b32_e32 v25, 0
	v_mov_b32_e32 v26, 0
	v_mov_b32_e32 v27, 0
	v_mov_b32_e32 v28, 0
	v_mov_b32_e32 v29, 0
	v_mov_b32_e32 v30, 0
	v_mov_b32_e32 v31, 0
	s_cmp_eq_u32 s43, 0
	s_cbranch_scc1 .Lp_fin
	s_mov_b32 s44, 0
.Lsub:
	ds_read_b64 v[36:37], v2
	v_cmp_gt_u32_e32 vcc, v3, v4
	v_add_u32_e32 v2, 64, v2
	v_add_u32_e32 v4, 16, v4
	v_mov_b32_e32 v33, 0x3c00
	s_waitcnt lgkmcnt(0)
	v_perm_b32 v32, v37, v36, v57
	v_cndmask_b32_e32 v33, 0, v33, vcc
	s_nop 0
	v_cndmask_b32_e32 v32, 0, v32, vcc
	s_nop 1
	v_mfma_f32_32x32x16_f16 v[96:111], v[32:35], v[64:67], 0
	v_mfma_f32_32x32x16_f16 v[112:127], v[32:35], v[68:71], 0
	s_nop 10
	v_add_f32_e64 v38, |v96|, |v97|
	v_add_f32_e64 v39, |v98|, |v99|
	v_add_f32_e64 v38, v38, |v100|
	v_add_f32_e64 v39, v39, |v101|
	v_add_f32_e64 v38, v38, |v102|
	v_add_f32_e64 v39, v39, |v103|
	v_add_f32_e64 v38, v38, |v104|
	v_add_f32_e64 v39, v39, |v105|
	v_add_f32_e64 v38, v38, |v106|
	v_add_f32_e64 v39, v39, |v107|
	v_add_f32_e64 v38, v38, |v108|
	v_add_f32_e64 v39, v39, |v109|
	v_add_f32_e64 v38, v38, |v110|
	v_add_f32_e64 v39, v39, |v111|
	v_add_f32_e32 v38, v38, v39
	v_add_f32_e32 v24, v24, v38
	v_mfma_f32_32x32x16_f16 v[96:111], v[32:35], v[72:75], 0
	v_add_f32_e64 v38, |v112|, |v113|
	v_add_f32_e64 v39, |v114|, |v115|
	v_add_f32_e64 v38, v38, |v116|
	v_add_f32_e64 v39, v39, |v117|
	v_add_f32_e64 v38, v38, |v118|
	v_add_f32_e64 v39, v39, |v119|
	v_add_f32_e64 v38, v38, |v120|
	v_add_f32_e64 v39, v39, |v121|
	v_add_f32_e64 v38, v38, |v122|
	v_add_f32_e64 v39, v39, |v123|
	v_add_f32_e64 v38, v38, |v124|
	v_add_f32_e64 v39, v39, |v125|
	v_add_f32_e64 v38, v38, |v126|
	v_add_f32_e64 v39, v39, |v127|
	v_add_f32_e32 v38, v38, v39
	v_add_f32_e32 v25, v25, v38
	v_mfma_f32_32x32x16_f16 v[112:127], v[32:35], v[76:79], 0
	v_add_f32_e64 v38, |v96|, |v97|
	v_add_f32_e64 v39, |v98|, |v99|
	v_add_f32_e64 v38, v38, |v100|
	v_add_f32_e64 v39, v39, |v101|
	v_add_f32_e64 v38, v38, |v102|
	v_add_f32_e64 v39, v39, |v103|
	v_add_f32_e64 v38, v38, |v104|
	v_add_f32_e64 v39, v39, |v105|
	v_add_f32_e64 v38, v38, |v106|
	v_add_f32_e64 v39, v39, |v107|
	v_add_f32_e64 v38, v38, |v108|
	v_add_f32_e64 v39, v39, |v109|
	v_add_f32_e64 v38, v38, |v110|
	v_add_f32_e64 v39, v39, |v111|
	v_add_f32_e32 v38, v38, v39
	v_add_f32_e32 v26, v26, v38
	v_mfma_f32_32x32x16_f16 v[96:111], v[32:35], v[80:83], 0
	v_add_f32_e64 v38, |v112|, |v113|
	v_add_f32_e64 v39, |v114|, |v115|
	v_add_f32_e64 v38, v38, |v116|
	v_add_f32_e64 v39, v39, |v117|
	v_add_f32_e64 v38, v38, |v118|
	v_add_f32_e64 v39, v39, |v119|
	v_add_f32_e64 v38, v38, |v120|
	v_add_f32_e64 v39, v39, |v121|
	v_add_f32_e64 v38, v38, |v122|
	v_add_f32_e64 v39, v39, |v123|
	v_add_f32_e64 v38, v38, |v124|
	v_add_f32_e64 v39, v39, |v125|
	v_add_f32_e64 v38, v38, |v126|
	v_add_f32_e64 v39, v39, |v127|
	v_add_f32_e32 v38, v38, v39
	v_add_f32_e32 v27, v27, v38
	v_mfma_f32_32x32x16_f16 v[112:127], v[32:35], v[84:87], 0
	v_add_f32_e64 v38, |v96|, |v97|
	v_add_f32_e64 v39, |v98|, |v99|
	v_add_f32_e64 v38, v38, |v100|
	v_add_f32_e64 v39, v39, |v101|
	v_add_f32_e64 v38, v38, |v102|
	v_add_f32_e64 v39, v39, |v103|
	v_add_f32_e64 v38, v38, |v104|
	v_add_f32_e64 v39, v39, |v105|
	v_add_f32_e64 v38, v38, |v106|
	v_add_f32_e64 v39, v39, |v107|
	v_add_f32_e64 v38, v38, |v108|
	v_add_f32_e64 v39, v39, |v109|
	v_add_f32_e64 v38, v38, |v110|
	v_add_f32_e64 v39, v39, |v111|
	v_add_f32_e32 v38, v38, v39
	v_add_f32_e32 v28, v28, v38
	v_mfma_f32_32x32x16_f16 v[96:111], v[32:35], v[88:91], 0
	v_add_f32_e64 v38, |v112|, |v113|
	v_add_f32_e64 v39, |v114|, |v115|
	v_add_f32_e64 v38, v38, |v116|
	v_add_f32_e64 v39, v39, |v117|
	v_add_f32_e64 v38, v38, |v118|
	v_add_f32_e64 v39, v39, |v119|
	v_add_f32_e64 v38, v38, |v120|
	v_add_f32_e64 v39, v39, |v121|
	v_add_f32_e64 v38, v38, |v122|
	v_add_f32_e64 v39, v39, |v123|
	v_add_f32_e64 v38, v38, |v124|
	v_add_f32_e64 v39, v39, |v125|
	v_add_f32_e64 v38, v38, |v126|
	v_add_f32_e64 v39, v39, |v127|
	v_add_f32_e32 v38, v38, v39
	v_add_f32_e32 v29, v29, v38
	v_mfma_f32_32x32x16_f16 v[112:127], v[32:35], v[92:95], 0
	v_add_f32_e64 v38, |v96|, |v97|
	v_add_f32_e64 v39, |v98|, |v99|
	v_add_f32_e64 v38, v38, |v100|
	v_add_f32_e64 v39, v39, |v101|
	v_add_f32_e64 v38, v38, |v102|
	v_add_f32_e64 v39, v39, |v103|
	v_add_f32_e64 v38, v38, |v104|
	v_add_f32_e64 v39, v39, |v105|
	v_add_f32_e64 v38, v38, |v106|
	v_add_f32_e64 v39, v39, |v107|
	v_add_f32_e64 v38, v38, |v108|
	v_add_f32_e64 v39, v39, |v109|
	v_add_f32_e64 v38, v38, |v110|
	v_add_f32_e64 v39, v39, |v111|
	v_add_f32_e32 v38, v38, v39
	v_add_f32_e32 v30, v30, v38
	v_add_f32_e64 v38, |v112|, |v113|
	v_add_f32_e64 v39, |v114|, |v115|
	v_add_f32_e64 v38, v38, |v116|
	v_add_f32_e64 v39, v39, |v117|
	v_add_f32_e64 v38, v38, |v118|
	v_add_f32_e64 v39, v39, |v119|
	v_add_f32_e64 v38, v38, |v120|
	v_add_f32_e64 v39, v39, |v121|
	v_add_f32_e64 v38, v38, |v122|
	v_add_f32_e64 v39, v39, |v123|
	v_add_f32_e64 v38, v38, |v124|
	v_add_f32_e64 v39, v39, |v125|
	v_add_f32_e64 v38, v38, |v126|
	v_add_f32_e64 v39, v39, |v127|
	v_add_f32_e32 v38, v38, v39
	v_add_f32_e32 v31, v31, v38
	s_add_i32 s44, s44, 1
	s_cmp_lt_u32 s44, s43
	s_cbranch_scc1 .Lsub
.Lp_fin:
	v_fma_mix_f32 v40, v7, v65, v24 op_sel_hi:[0,1,0]
	v_fma_mix_f32 v40, v6, v64, v40 op_sel:[0,1,0] op_sel_hi:[0,1,0]
	v_fma_mix_f32 v40, v5, v64, v40 op_sel_hi:[0,1,0]
	v_mul_f32_e32 v40, v8, v40
	v_cvt_f16_f32_e32 v40, v40
	ds_write_b16 v9, v40 offset:0
	v_fma_mix_f32 v41, v7, v69, v25 op_sel_hi:[0,1,0]
	v_fma_mix_f32 v41, v6, v68, v41 op_sel:[0,1,0] op_sel_hi:[0,1,0]
	v_fma_mix_f32 v41, v5, v68, v41 op_sel_hi:[0,1,0]
	v_mul_f32_e32 v41, v8, v41
	v_cvt_f16_f32_e32 v41, v41
	ds_write_b16 v9, v41 offset:64
	v_fma_mix_f32 v40, v7, v73, v26 op_sel_hi:[0,1,0]
	v_fma_mix_f32 v40, v6, v72, v40 op_sel:[0,1,0] op_sel_hi:[0,1,0]
	v_fma_mix_f32 v40, v5, v72, v40 op_sel_hi:[0,1,0]
	v_mul_f32_e32 v40, v8, v40
	v_cvt_f16_f32_e32 v40, v40
	ds_write_b16 v9, v40 offset:128
	v_fma_mix_f32 v41, v7, v77, v27 op_sel_hi:[0,1,0]
	v_fma_mix_f32 v41, v6, v76, v41 op_sel:[0,1,0] op_sel_hi:[0,1,0]
	v_fma_mix_f32 v41, v5, v76, v41 op_sel_hi:[0,1,0]
	v_mul_f32_e32 v41, v8, v41
	v_cvt_f16_f32_e32 v41, v41
	ds_write_b16 v9, v41 offset:192
	v_fma_mix_f32 v40, v7, v81, v28 op_sel_hi:[0,1,0]
	v_fma_mix_f32 v40, v6, v80, v40 op_sel:[0,1,0] op_sel_hi:[0,1,0]
	v_fma_mix_f32 v40, v5, v80, v40 op_sel_hi:[0,1,0]
	v_mul_f32_e32 v40, v8, v40
	v_cvt_f16_f32_e32 v40, v40
	ds_write_b16 v9, v40 offset:256
	v_fma_mix_f32 v41, v7, v85, v29 op_sel_hi:[0,1,0]
	v_fma_mix_f32 v41, v6, v84, v41 op_sel:[0,1,0] op_sel_hi:[0,1,0]
	v_fma_mix_f32 v41, v5, v84, v41 op_sel_hi:[0,1,0]
	v_mul_f32_e32 v41, v8, v41
	v_cvt_f16_f32_e32 v41, v41
	ds_write_b16 v9, v41 offset:320
	v_fma_mix_f32 v40, v7, v89, v30 op_sel_hi:[0,1,0]
	v_fma_mix_f32 v40, v6, v88, v40 op_sel:[0,1,0] op_sel_hi:[0,1,0]
	v_fma_mix_f32 v40, v5, v88, v40 op_sel_hi:[0,1,0]
	v_mul_f32_e32 v40, v8, v40
	v_cvt_f16_f32_e32 v40, v40
	ds_write_b16 v9, v40 offset:384
	v_fma_mix_f32 v41, v7, v93, v31 op_sel_hi:[0,1,0]
	v_fma_mix_f32 v41, v6, v92, v41 op_sel:[0,1,0] op_sel_hi:[0,1,0]
	v_fma_mix_f32 v41, v5, v92, v41 op_sel_hi:[0,1,0]
	v_mul_f32_e32 v41, v8, v41
	v_cvt_f16_f32_e32 v41, v41
	ds_write_b16 v9, v41 offset:448
	s_branch .Lp_next
.Lp_done:
	v_xor_b32_e32 v102, 16, v18
	v_lshlrev_b32_e32 v102, 2, v102
	s_branch .LBB3_67

	.amdhsa_kernel _Z6k_mainPKiPKjPK15HIP_vector_typeIfLj2EEPKfS8_PKDF16_S8_Pf
		.amdhsa_group_segment_fixed_size 144224
		.amdhsa_private_segment_fixed_size 0
		.amdhsa_kernarg_size 64
		.amdhsa_user_sgpr_count 2
		.amdhsa_user_sgpr_dispatch_ptr 0
		.amdhsa_user_sgpr_queue_ptr 0
		.amdhsa_user_sgpr_kernarg_segment_ptr 1
		.amdhsa_user_sgpr_dispatch_id 0
		.amdhsa_user_sgpr_kernarg_preload_length 0
		.amdhsa_user_sgpr_kernarg_preload_offset 0
		.amdhsa_user_sgpr_private_segment_size 0
		.amdhsa_uses_dynamic_stack 0
		.amdhsa_enable_private_segment 0
		.amdhsa_system_sgpr_workgroup_id_x 1
		.amdhsa_system_sgpr_workgroup_id_y 0
		.amdhsa_system_sgpr_workgroup_id_z 0
		.amdhsa_system_sgpr_workgroup_info 0
		.amdhsa_system_vgpr_workitem_id 0
		.amdhsa_next_free_vgpr 128
		.amdhsa_next_free_sgpr 96
		.amdhsa_accum_offset 128
		.amdhsa_reserve_vcc 1
		.amdhsa_float_round_mode_32 0
		.amdhsa_float_round_mode_16_64 0
		.amdhsa_float_denorm_mode_32 3
		.amdhsa_float_denorm_mode_16_64 3
		.amdhsa_dx10_clamp 1
		.amdhsa_ieee_mode 1
		.amdhsa_fp16_overflow 0
		.amdhsa_tg_split 0
		.amdhsa_exception_fp_ieee_invalid_op 0
		.amdhsa_exception_fp_denorm_src 0
		.amdhsa_exception_fp_ieee_div_zero 0
		.amdhsa_exception_fp_ieee_overflow 0
		.amdhsa_exception_fp_ieee_underflow 0
		.amdhsa_exception_fp_ieee_inexact 0
		.amdhsa_exception_int_div_zero 0
	.end_amdhsa_kernel

amdhsa.kernels:
  - .agpr_count:     0
    .args:
      - .actual_access:  read_only
        .address_space:  global
        .offset:         0
        .size:           8
        .value_kind:     global_buffer
      - .actual_access:  read_only
        .address_space:  global
        .offset:         8
        .size:           8
        .value_kind:     global_buffer
      - .actual_access:  write_only
        .address_space:  global
        .offset:         16
        .size:           8
        .value_kind:     global_buffer
      - .actual_access:  write_only
        .address_space:  global
        .offset:         24
        .size:           8
        .value_kind:     global_buffer
      - .actual_access:  write_only
        .address_space:  global
        .offset:         32
        .size:           8
        .value_kind:     global_buffer
      - .actual_access:  write_only
        .address_space:  global
        .offset:         40
        .size:           8
        .value_kind:     global_buffer
      - .actual_access:  write_only
        .address_space:  global
        .offset:         48
        .size:           8
        .value_kind:     global_buffer
      - .actual_access:  write_only
        .address_space:  global
        .offset:         56
        .size:           8
        .value_kind:     global_buffer
      - .actual_access:  read_only
        .address_space:  global
        .offset:         64
        .size:           8
        .value_kind:     global_buffer
      - .actual_access:  write_only
        .address_space:  global
        .offset:         72
        .size:           8
        .value_kind:     global_buffer
    .group_segment_fixed_size: 18800
    .kernarg_segment_align: 8
    .kernarg_segment_size: 80
    .language:       OpenCL C
    .language_version:
      - 2
      - 0
    .max_flat_workgroup_size: 1024
    .name:           _Z6k_partPKiS0_PjPhS1_S1_PfS3_PKfPDF16_
    .private_segment_fixed_size: 0
    .sgpr_count:     48
    .sgpr_spill_count: 0
    .symbol:         _Z6k_partPKiS0_PjPhS1_S1_PfS3_PKfPDF16_.kd
    .uniform_work_group_size: 1
    .uses_dynamic_stack: false
    .vgpr_count:     40
    .vgpr_spill_count: 0
    .wavefront_size: 64
  - .agpr_count:     0
    .args:
      - .actual_access:  read_only
        .address_space:  global
        .offset:         0
        .size:           8
        .value_kind:     global_buffer
      - .actual_access:  read_only
        .address_space:  global
        .offset:         8
        .size:           8
        .value_kind:     global_buffer
      - .actual_access:  read_only
        .address_space:  global
        .offset:         16
        .size:           8
        .value_kind:     global_buffer
      - .actual_access:  read_only
        .address_space:  global
        .offset:         24
        .size:           8
        .value_kind:     global_buffer
      - .actual_access:  write_only
        .address_space:  global
        .offset:         32
        .size:           8
        .value_kind:     global_buffer
      - .actual_access:  write_only
        .address_space:  global
        .offset:         40
        .size:           8
        .value_kind:     global_buffer
    .group_segment_fixed_size: 3076
    .kernarg_segment_align: 8
    .kernarg_segment_size: 48
    .language:       OpenCL C
    .language_version:
      - 2
      - 0
    .max_flat_workgroup_size: 512
    .name:           _Z5k_degPKjPKhS0_S0_P15HIP_vector_typeIiLj2EEPi
    .private_segment_fixed_size: 0
    .sgpr_count:     74
    .sgpr_spill_count: 0
    .symbol:         _Z5k_degPKjPKhS0_S0_P15HIP_vector_typeIiLj2EEPi.kd
    .uniform_work_group_size: 1
    .uses_dynamic_stack: false
    .vgpr_count:     61
    .vgpr_spill_count: 0
    .wavefront_size: 64
  - .agpr_count:     0
    .args:
      - .actual_access:  read_only
        .address_space:  global
        .offset:         0
        .size:           8
        .value_kind:     global_buffer
      - .actual_access:  read_only
        .address_space:  global
        .offset:         8
        .size:           8
        .value_kind:     global_buffer
      - .actual_access:  read_only
        .address_space:  global
        .offset:         16
        .size:           8
        .value_kind:     global_buffer
      - .actual_access:  read_only
        .address_space:  global
        .offset:         24
        .size:           8
        .value_kind:     global_buffer
      - .actual_access:  write_only
        .address_space:  global
        .offset:         32
        .size:           8
        .value_kind:     global_buffer
      - .actual_access:  write_only
        .address_space:  global
        .offset:         40
        .size:           8
        .value_kind:     global_buffer
      - .actual_access:  write_only
        .address_space:  global
        .offset:         48
        .size:           8
        .value_kind:     global_buffer
    .group_segment_fixed_size: 4128
    .kernarg_segment_align: 8
    .kernarg_segment_size: 56
    .language:       OpenCL C
    .language_version:
      - 2
      - 0
    .max_flat_workgroup_size: 256
    .name:           _Z5k_csrPKjS0_PK15HIP_vector_typeIiLj2EEPKiPiPjPS1_IfLj2EE
    .private_segment_fixed_size: 0
    .sgpr_count:     74
    .sgpr_spill_count: 0
    .symbol:         _Z5k_csrPKjS0_PK15HIP_vector_typeIiLj2EEPKiPiPjPS1_IfLj2EE.kd
    .uniform_work_group_size: 1
    .uses_dynamic_stack: false
    .vgpr_count:     122
    .vgpr_spill_count: 0
    .wavefront_size: 64
  - .agpr_count:     0
    .args:
      - .actual_access:  read_only
        .address_space:  global
        .offset:         0
        .size:           8
        .value_kind:     global_buffer
      - .actual_access:  read_only
        .address_space:  global
        .offset:         8
        .size:           8
        .value_kind:     global_buffer
      - .actual_access:  read_only
        .address_space:  global
        .offset:         16
        .size:           8
        .value_kind:     global_buffer
      - .actual_access:  read_only
        .address_space:  global
        .offset:         24
        .size:           8
        .value_kind:     global_buffer
      - .actual_access:  read_only
        .address_space:  global
        .offset:         32
        .size:           8
        .value_kind:     global_buffer
      - .actual_access:  read_only
        .address_space:  global
        .offset:         40
        .size:           8
        .value_kind:     global_buffer
      - .actual_access:  read_only
        .address_space:  global
        .offset:         48
        .size:           8
        .value_kind:     global_buffer
      - .address_space:  global
        .offset:         56
        .size:           8
        .value_kind:     global_buffer
    .group_segment_fixed_size: 144224
    .kernarg_segment_align: 8
    .kernarg_segment_size: 64
    .language:       OpenCL C
    .language_version:
      - 2
      - 0
    .max_flat_workgroup_size: 1024
    .name:           _Z6k_mainPKiPKjPK15HIP_vector_typeIfLj2EEPKfS8_PKDF16_S8_Pf
    .private_segment_fixed_size: 0
    .sgpr_count:     84
    .sgpr_spill_count: 0
    .symbol:         _Z6k_mainPKiPKjPK15HIP_vector_typeIfLj2EEPKfS8_PKDF16_S8_Pf.kd
    .uniform_work_group_size: 1
    .uses_dynamic_stack: false
    .vgpr_count:     128
    .vgpr_spill_count: 0
    .wavefront_size: 64
  - .agpr_count:     0
    .args:
      - .actual_access:  read_only
        .address_space:  global
        .offset:         0
        .size:           8
        .value_kind:     global_buffer
      - .actual_access:  read_only
        .address_space:  global
        .offset:         8
        .size:           8
        .value_kind:     global_buffer
      - .actual_access:  read_only
        .address_space:  global
        .offset:         16
        .size:           8
        .value_kind:     global_buffer
      - .actual_access:  read_only
        .address_space:  global
        .offset:         24
        .size:           8
        .value_kind:     global_buffer
      - .actual_access:  read_only
        .address_space:  global
        .offset:         32
        .size:           8
        .value_kind:     global_buffer
      - .actual_access:  read_only
        .address_space:  global
        .offset:         40
        .size:           8
        .value_kind:     global_buffer
      - .actual_access:  read_only
        .address_space:  global
        .offset:         48
        .size:           8
        .value_kind:     global_buffer
      - .actual_access:  read_only
        .address_space:  global
        .offset:         56
        .size:           8
        .value_kind:     global_buffer
      - .actual_access:  read_only
        .address_space:  global
        .offset:         64
        .size:           8
        .value_kind:     global_buffer
      - .actual_access:  read_only
        .address_space:  global
        .offset:         72
        .size:           8
        .value_kind:     global_buffer
      - .address_space:  global
        .offset:         80
        .size:           8
        .value_kind:     global_buffer
    .group_segment_fixed_size: 2688
    .kernarg_segment_align: 8
    .kernarg_segment_size: 88
    .language:       OpenCL C
    .language_version:
      - 2
      - 0
    .max_flat_workgroup_size: 256
    .name:           _Z7k_finalPKfS0_S0_S0_S0_S0_S0_S0_S0_S0_Pf
    .private_segment_fixed_size: 0
    .sgpr_count:     36
    .sgpr_spill_count: 0
    .symbol:         _Z7k_finalPKfS0_S0_S0_S0_S0_S0_S0_S0_S0_Pf.kd
    .uniform_work_group_size: 1
    .uses_dynamic_stack: false
    .vgpr_count:     98
    .vgpr_spill_count: 0
    .wavefront_size: 64
